# s14 + small_from_hn: bias load hoisted to the top; closing barrier no longer waits for the small[] store acks
# baseline (speedup 1.0000x reference)
; #define PG8_LAS __attribute__((address_space(3)))
; __device__ __forceinline__ void small_from_hn(const h16* __restrict__ hn, const h16* __restrict__ wsm16  , const float* __restrict__ fox_bf, const float* __restrict__ ml_bi, ...
;     int tid_ = threadIdx.x; asm volatile("" : "+v"(tid_));
;     const int lane = tid_ & 63, wave = tid_ >> 6;
;     constexpr int WP = 1032;
; #pragma unroll
;     for (int q = 0; q < 4; ++q) { const int e = (q * NTHREADS + tid_) * 8, c = e >> 10, k = e & 1023;
;         *(PG8_LAS h16x8*)(L + (c * WP + k) * 2) = *(const h16x8*)(wsm16 + e); }
;     asm volatile("s_waitcnt vmcnt(0) lgkmcnt(0)" ::: "memory"); __syncthreads();
;     if (wave < 4) {
;         for (int blk = blockIdx.x; blk < TH / 64; blk += gridDim.x) {
;             const int R0 = blk * 64 + 16 * wave, i = lane & 15, gq = lane >> 4;
;             const h16* xr = hn + (size_t)(R0 + i) * DM + 8 * gq;
;             const PG8_LAS unsigned char* wr = L + (i * WP + 8 * gq) * 2;
;             f32x4 acc = {0.f, 0.f, 0.f, 0.f};
; #pragma unroll 1
;             for (int kb = 0; kb < 32; kb += 16) {
;                 h16x8 av[16];
; #pragma unroll
;                 for (int u = 0; u < 16; ++u) av[u] = *(const h16x8*)(xr + 32 * (kb + u));
;                 asm volatile("" ::: "memory");
; #pragma unroll
;                 for (int u = 0; u < 16; ++u) { const h16x8 bv = *(const PG8_LAS h16x8*)(wr + 64 * (kb + u));
;                     acc = __builtin_amdgcn_mfma_f32_16x16x32_f16(av[u], bv, acc, 0, 0, 0); }
;             }
;             const float bias = i < 8 ? fox_bf[i] : i < 12 ? ml_bi[i - 8] : ml_bf[i - 12];
.LBB0_932:
	v_readlane_b32 s0, v255, 32
	s_cmp_eq_u32 s0, 1
	s_cbranch_scc0 .LBB0_1000
	v_readlane_b32 s0, v255, 31
	s_cmp_lt_u32 s0, 2
	v_readlane_b32 s0, v253, 54
	v_readlane_b32 s2, v253, 56
	v_readlane_b32 s1, v253, 55
	s_cselect_b32 s0, s0, s2
	v_readlane_b32 s2, v253, 57
	s_cselect_b32 s1, s1, s2
	v_readlane_b32 s2, v255, 42
	s_cmp_eq_u32 s2, 0
	v_readlane_b32 s2, v253, 24
	v_readlane_b32 s3, v253, 25
	s_cselect_b32 s3, s3, s1
	s_cselect_b32 s2, s2, s0
	v_readlane_b32 s0, v255, 36
	s_lshl_b32 s0, s0, 15
	v_readlane_b32 s4, v254, 2
	v_mov_b32_e32 v0, v243
	v_readlane_b32 s1, v255, 37
	v_readlane_b32 s5, v254, 3
	s_add_u32 s0, s4, s0
	s_addc_u32 s1, s5, 0
	v_lshlrev_b32_e32 v6, 3, v0
	v_ashrrev_i32_e32 v7, 31, v6
	v_lshl_add_u64 v[2:3], v[6:7], 1, s[0:1]
	global_load_dwordx4 v[2:5], v[2:3], off
	v_and_b32_e32 v1, 0x3f8, v6
	v_bfe_i32 v8, v0, 7, 22
	s_movk_i32 s4, 0x408
	v_mad_i32_i24 v7, v8, s4, v1
	v_lshl_add_u32 v7, v7, 1, 0
	v_add_u32_e32 v12, 0x1000, v6
	v_ashrrev_i32_e32 v13, 31, v12
	v_ashrrev_i32_e32 v9, 10, v12
	v_lshl_add_u64 v[12:13], v[12:13], 1, s[0:1]
	global_load_dwordx4 v[12:15], v[12:13], off
	v_mad_i32_i24 v9, v9, s4, v1
	v_lshl_add_u32 v9, v9, 1, 0
	v_add_u32_e32 v16, 0x2000, v6
	v_ashrrev_i32_e32 v17, 31, v16
	v_ashrrev_i32_e32 v10, 10, v16
	v_lshl_add_u64 v[16:17], v[16:17], 1, s[0:1]
	global_load_dwordx4 v[16:19], v[16:17], off
	v_mad_i32_i24 v10, v10, s4, v1
	v_lshl_add_u32 v10, v10, 1, 0
	v_add_u32_e32 v20, 0x3000, v6
	v_ashrrev_i32_e32 v21, 31, v20
	v_ashrrev_i32_e32 v6, 10, v20
	v_lshl_add_u64 v[20:21], v[20:21], 1, s[0:1]
	global_load_dwordx4 v[20:23], v[20:21], off
	v_mad_i32_i24 v1, v6, s4, v1
	v_lshl_add_u32 v1, v1, 1, 0
	v_readlane_b32 s0, v254, 63
	v_readlane_b32 s1, v255, 0
	s_waitcnt vmcnt(3)
	ds_write_b128 v7, v[2:5]
	s_waitcnt vmcnt(2)
	ds_write_b128 v9, v[12:15]
	s_waitcnt vmcnt(1)
	ds_write_b128 v10, v[16:19]
	s_waitcnt vmcnt(0)
	ds_write_b128 v1, v[20:23]
	v_ashrrev_i32_e32 v1, 6, v0
	s_waitcnt vmcnt(0) lgkmcnt(0)
	v_cmp_gt_i32_e32 vcc, 4, v1
	s_and_b64 s[0:1], vcc, s[0:1]
	s_waitcnt lgkmcnt(0)
	s_barrier
	s_and_saveexec_b64 s[14:15], s[0:1]
	s_cbranch_execz .LBB0_971
	v_readlane_b32 s0, v255, 36
	v_readlane_b32 s1, v255, 37
	s_lshl_b32 s28, s0, 2
	v_readlane_b32 s52, v253, 36
	s_mov_b32 s6, s0
	s_lshl_b64 s[0:1], s[28:29], 2
	v_readlane_b32 s64, v253, 48
	v_readlane_b32 s65, v253, 49
	s_add_u32 s4, s64, s0
	v_readlane_b32 s62, v253, 46
	s_addc_u32 s5, s65, s1
	v_lshlrev_b32_e32 v76, 4, v1
	v_and_b32_e32 v77, 15, v0
	v_bfe_u32 v1, v0, 4, 2
	v_readlane_b32 s63, v253, 47
	s_add_u32 s0, s62, s0
	v_lshlrev_b32_e32 v96, 4, v1
	v_mul_u32_u24_e32 v2, 0x408, v77
	s_addc_u32 s1, s63, s1
	s_lshl_b32 s28, s6, 3
	v_lshl_add_u64 v[68:69], s[2:3], 0, v[96:97]
	v_lshl_add_u32 v2, v1, 3, v2
	v_lshlrev_b32_e32 v96, 2, v77
	v_readlane_b32 s58, v253, 42
	s_lshl_b64 s[10:11], s[28:29], 2
	v_lshl_add_u32 v78, v2, 1, 0
	v_lshl_add_u64 v[2:3], s[4:5], 0, v[96:97]
	s_movk_i32 s4, 0xffd0
	v_lshl_add_u64 v[4:5], s[0:1], 0, v[96:97]
	s_movk_i32 s0, 0xffe0
	v_readlane_b32 s59, v253, 43
	s_add_u32 s10, s58, s10
	s_mov_b32 s5, -1
	s_mov_b32 s1, -1
	s_addc_u32 s11, s59, s11
	v_lshl_add_u64 v[2:3], v[2:3], 0, s[4:5]
	v_lshl_add_u64 v[4:5], v[4:5], 0, s[0:1]
	v_and_b32_e32 v0, 12, v0
	v_readlane_b32 s0, v255, 43
	v_cmp_gt_u32_e32 vcc, 12, v77
	v_lshl_add_u64 v[6:7], s[10:11], 0, v[96:97]
	v_cmp_ne_u32_e64 s[38:39], 8, v0
	v_lshl_or_b32 v79, v1, 2, s0
	v_cndmask_b32_e32 v0, v2, v4, vcc
	v_cndmask_b32_e32 v1, v3, v5, vcc
	v_cmp_gt_u32_e32 vcc, 8, v77
	v_lshl_add_u64 v[70:71], s[86:87], 0, v[96:97]
	v_readlane_b32 s4, v252, 0
	v_cndmask_b32_e32 v73, v1, v7, vcc
	v_cndmask_b32_e32 v72, v0, v6, vcc
	global_load_dword v120, v[72:73], off
	v_readlane_b32 s53, v253, 37
	v_readlane_b32 s54, v253, 38
	v_readlane_b32 s55, v253, 39
	v_readlane_b32 s56, v253, 40
	v_readlane_b32 s57, v253, 41
	v_readlane_b32 s60, v253, 44
	v_readlane_b32 s61, v253, 45
	v_readlane_b32 s66, v253, 50
	v_readlane_b32 s67, v253, 51
	s_branch .LBB0_946

; #define PG8_LAS __attribute__((address_space(3)))
; __device__ __forceinline__ void small_from_hn(const h16* __restrict__ hn, const h16* __restrict__ wsm16  , const float* __restrict__ fox_bf, const float* __restrict__ ml_bi, ...
;     ...
;             for (int kb = 0; kb < 32; kb += 16) {
;                 h16x8 av[16];
; #pragma unroll
;                 for (int u = 0; u < 16; ++u) av[u] = *(const h16x8*)(xr + 32 * (kb + u));
;                 asm volatile("" ::: "memory");
; #pragma unroll
;                 for (int u = 0; u < 16; ++u) { const h16x8 bv = *(const PG8_LAS h16x8*)(wr + 64 * (kb + u));
;                     acc = __builtin_amdgcn_mfma_f32_16x16x32_f16(av[u], bv, acc, 0, 0, 0); }
;             }
;             const float bias = i < 8 ? fox_bf[i] : i < 12 ? ml_bi[i - 8] : ml_bf[i - 12];
; #pragma unroll
;             for (int r = 0; r < 4; ++r) {
;                 const float pre = acc[r] + bias;
;                 small[(size_t)(row0 + R0 + 4 * gq + r) * 16 + i] = (i >= 8 && i < 12) ? pre : log_sigmoidf_(pre);
.LBB0_947:
	v_cndmask_b32_e64 v4, 0, 1, s[0:1]
	s_lshl_b32 s28, s5, 6
	v_cmp_ne_u32_e32 vcc, 1, v4
	v_lshl_add_u64 v[4:5], v[74:75], 0, s[28:29]
	global_load_dwordx4 v[4:7], v[4:5], off
	s_or_b32 s68, s28, 64
	s_mov_b32 s69, s29
	v_lshl_add_u64 v[8:9], v[74:75], 0, s[68:69]
	global_load_dwordx4 v[52:55], v[8:9], off
	s_or_b32 s66, s28, 0x80
	s_mov_b32 s67, s29
	v_lshl_add_u64 v[8:9], v[74:75], 0, s[66:67]
	global_load_dwordx4 v[48:51], v[8:9], off
	s_or_b32 s40, s28, 0x340
	s_mov_b32 s41, s29
	s_or_b32 s64, s28, 0xc0
	s_mov_b32 s65, s29
	v_lshl_add_u64 v[56:57], v[74:75], 0, s[40:41]
	global_load_dwordx4 v[64:67], v[56:57], off
	v_lshl_add_u64 v[8:9], v[74:75], 0, s[64:65]
	global_load_dwordx4 v[44:47], v[8:9], off
	s_or_b32 s20, s28, 0x380
	s_mov_b32 s21, s29
	s_or_b32 s62, s28, 0x100
	s_mov_b32 s63, s29
	v_lshl_add_u64 v[56:57], v[74:75], 0, s[20:21]
	global_load_dwordx4 v[56:59], v[56:57], off
	v_lshl_add_u64 v[8:9], v[74:75], 0, s[62:63]
	global_load_dwordx4 v[40:43], v[8:9], off
	s_or_b32 s0, s28, 0x3c0
	s_mov_b32 s1, s29
	s_or_b32 s60, s28, 0x140
	s_mov_b32 s61, s29
	v_lshl_add_u64 v[60:61], v[74:75], 0, s[0:1]
	global_load_dwordx4 v[60:63], v[60:61], off
	v_lshl_add_u64 v[8:9], v[74:75], 0, s[60:61]
	global_load_dwordx4 v[36:39], v[8:9], off
	s_or_b32 s58, s28, 0x180
	s_mov_b32 s59, s29
	v_lshl_add_u64 v[8:9], v[74:75], 0, s[58:59]
	global_load_dwordx4 v[32:35], v[8:9], off
	s_or_b32 s56, s28, 0x1c0
	s_mov_b32 s57, s29
	v_lshl_add_u64 v[8:9], v[74:75], 0, s[56:57]
	global_load_dwordx4 v[28:31], v[8:9], off
	s_or_b32 s54, s28, 0x200
	s_mov_b32 s55, s29
	v_lshl_add_u64 v[8:9], v[74:75], 0, s[54:55]
	global_load_dwordx4 v[24:27], v[8:9], off
	s_or_b32 s52, s28, 0x240
	s_mov_b32 s53, s29
	v_lshl_add_u64 v[8:9], v[74:75], 0, s[52:53]
	global_load_dwordx4 v[20:23], v[8:9], off
	s_or_b32 s50, s28, 0x280
	s_mov_b32 s51, s29
	v_lshl_add_u64 v[8:9], v[74:75], 0, s[50:51]
	global_load_dwordx4 v[16:19], v[8:9], off
	s_or_b32 s46, s28, 0x2c0
	s_mov_b32 s47, s29
	v_lshl_add_u64 v[8:9], v[74:75], 0, s[46:47]
	global_load_dwordx4 v[12:15], v[8:9], off
	s_or_b32 s42, s28, 0x300
	s_mov_b32 s43, s29
	v_lshl_add_u64 v[8:9], v[74:75], 0, s[42:43]
	global_load_dwordx4 v[8:11], v[8:9], off
	v_add_u32_e32 v81, s28, v78
	ds_read_b128 v[82:85], v81
	s_mov_b32 s5, 16
	s_and_b64 vcc, exec, vcc
	s_waitcnt vmcnt(15) lgkmcnt(0)
	v_mfma_f32_16x16x32_f16 v[0:3], v[4:7], v[82:85], v[0:3]
	v_add_u32_e32 v4, s68, v78
	ds_read_b128 v[4:7], v4
	s_waitcnt vmcnt(14) lgkmcnt(0)
	v_mfma_f32_16x16x32_f16 v[0:3], v[52:55], v[4:7], v[0:3]
	v_add_u32_e32 v4, s66, v78
	ds_read_b128 v[4:7], v4
	s_waitcnt vmcnt(13) lgkmcnt(0)
	v_mfma_f32_16x16x32_f16 v[0:3], v[48:51], v[4:7], v[0:3]
	v_add_u32_e32 v4, s64, v78
	ds_read_b128 v[4:7], v4
	s_waitcnt vmcnt(11) lgkmcnt(0)
	v_mfma_f32_16x16x32_f16 v[0:3], v[44:47], v[4:7], v[0:3]
	v_add_u32_e32 v4, s62, v78
	ds_read_b128 v[4:7], v4
	s_waitcnt vmcnt(9) lgkmcnt(0)
	v_mfma_f32_16x16x32_f16 v[0:3], v[40:43], v[4:7], v[0:3]
	v_add_u32_e32 v4, s60, v78
	ds_read_b128 v[4:7], v4
	s_waitcnt vmcnt(7) lgkmcnt(0)
	v_mfma_f32_16x16x32_f16 v[0:3], v[36:39], v[4:7], v[0:3]
	v_add_u32_e32 v4, s58, v78
	ds_read_b128 v[4:7], v4
	s_waitcnt vmcnt(6) lgkmcnt(0)
	v_mfma_f32_16x16x32_f16 v[0:3], v[32:35], v[4:7], v[0:3]
	v_add_u32_e32 v4, s56, v78
	ds_read_b128 v[4:7], v4
	s_waitcnt vmcnt(5) lgkmcnt(0)
	v_mfma_f32_16x16x32_f16 v[0:3], v[28:31], v[4:7], v[0:3]
	v_add_u32_e32 v4, s54, v78
	ds_read_b128 v[4:7], v4
	s_waitcnt vmcnt(4) lgkmcnt(0)
	v_mfma_f32_16x16x32_f16 v[0:3], v[24:27], v[4:7], v[0:3]
	v_add_u32_e32 v4, s52, v78
	ds_read_b128 v[4:7], v4
	s_waitcnt vmcnt(3) lgkmcnt(0)
	v_mfma_f32_16x16x32_f16 v[0:3], v[20:23], v[4:7], v[0:3]
	v_add_u32_e32 v4, s50, v78
	ds_read_b128 v[4:7], v4
	s_waitcnt vmcnt(2) lgkmcnt(0)
	v_mfma_f32_16x16x32_f16 v[0:3], v[16:19], v[4:7], v[0:3]
	v_add_u32_e32 v4, s46, v78
	ds_read_b128 v[4:7], v4
	s_waitcnt vmcnt(1) lgkmcnt(0)
	v_mfma_f32_16x16x32_f16 v[0:3], v[12:15], v[4:7], v[0:3]
	v_add_u32_e32 v4, s42, v78
	ds_read_b128 v[4:7], v4
	s_waitcnt vmcnt(0) lgkmcnt(0)
	v_mfma_f32_16x16x32_f16 v[0:3], v[8:11], v[4:7], v[0:3]
	v_add_u32_e32 v4, s40, v78
	ds_read_b128 v[4:7], v4
	s_waitcnt lgkmcnt(0)
	v_mfma_f32_16x16x32_f16 v[0:3], v[64:67], v[4:7], v[0:3]
	v_add_u32_e32 v4, s20, v78
	ds_read_b128 v[4:7], v4
	s_waitcnt lgkmcnt(0)
	v_mfma_f32_16x16x32_f16 v[0:3], v[56:59], v[4:7], v[0:3]
	v_add_u32_e32 v4, s0, v78
	ds_read_b128 v[4:7], v4
	s_mov_b64 s[0:1], 0
	s_waitcnt lgkmcnt(0)
	v_mfma_f32_16x16x32_f16 v[0:3], v[60:63], v[4:7], v[0:3]
	s_cbranch_vccz .LBB0_947
	v_mov_b32_e32 v6, v120
	s_waitcnt vmcnt(0)
	s_nop 4
	v_add_f32_e32 v0, v0, v6
	s_and_saveexec_b64 s[20:21], s[38:39]
	s_cbranch_execz .LBB0_954
	s_mov_b32 s0, 0xbfb8aa3b
	v_mul_f32_e64 v4, |v0|, s0
	v_exp_f32_e32 v5, v4
	s_mov_b32 s0, 0x3c23d70a
	v_cmp_ngt_f32_e32 vcc, s0, v5
	s_and_saveexec_b64 s[0:1], vcc
	s_xor_b64 s[40:41], exec, s[0:1]
	s_cbranch_execz .LBB0_951
	v_add_f32_e32 v4, 1.0, v5
	v_cmp_gt_f32_e32 vcc, s44, v4
	s_mov_b32 s0, 0x3f317217
	s_nop 0
	v_cndmask_b32_e64 v5, 0, 32, vcc
	v_ldexp_f32 v4, v4, v5
	v_log_f32_e32 v4, v4
	s_nop 0
	v_mul_f32_e32 v5, 0x3f317217, v4
	v_fma_f32 v5, v4, s0, -v5
	v_fmac_f32_e32 v5, 0x3377d1cf, v4
	s_mov_b32 s0, 0x7f800000
	v_fmac_f32_e32 v5, 0x3f317217, v4
	v_cmp_lt_f32_e64 s[0:1], |v4|, s0
	s_nop 1
	v_cndmask_b32_e64 v4, v4, v5, s[0:1]
	v_cndmask_b32_e32 v5, 0, v244, vcc
	v_sub_f32_e32 v4, v4, v5

;     __device__ bool next(int i, Unit& u) const { const long L = (long)i * G + c; if (L >= nwg) return false; tile_of((int)L, nM, nN, u.pm, u.pn, wgm); u.z = 0; return true; }
; #define PG8_BAR __builtin_amdgcn_s_barrier()
; #define PG8_BAR __builtin_amdgcn_s_barrier()
; template <class Epi, class Sched, bool ALIGN_EPI = true>
; __device__ __forceinline__ void gemm_phase(PG8_LAS unsigned char* lds, const Gemm g, const Sched& S, const Epi& E) {
;     ...
;     const int tid = tid_, wid = __builtin_amdgcn_readfirstlane(tid >> 6), lane = tid & 63, wr = wid >> 2, wc = wid & 3, fr = lane & 15, fq = lane >> 4;
;     const int nt = g.K / BK;
;     unsigned voffA[2], voffB[2];
; #pragma unroll
;     for (int i = 0; i < 2; ++i) { int R, C; stage_rc(tid * 16 + i * 8192, R, C); const int Rb = Epi::PERM ? ((R & ~31) + perm32(R & 31)) : R;
;         voffA[i] = (unsigned)(R * g.lda + C) * 2u; voffB[i] = (unsigned)(Rb * g.ldb + C) * 2u; }
;     const size_t kstep = (size_t)(BK * 2);
;     const size_t hA = (size_t)HALF * g.lda * 2, hB = (size_t)HALF * g.ldb * 2;
;     const size_t tA = 2 * hA, tB = 2 * hB;
;     const unsigned ldsw = (unsigned)wid * 1024u;
;     const int aoff = lds_byte(wr * 64 + fr, fq * 8), boff = lds_byte(wc * 32 + fr, fq * 8);
;     ...
;     Unit cur, nxt; int ui = 0;
;     if (!S.next(0, cur)) return;
;     f32x4 acc[2][2][4][2];
; #pragma unroll
;     for (int a = 0; a < 2; ++a)
; #pragma unroll
;         for (int b = 0; b < 2; ++b)
; #pragma unroll
;             for (int m = 0; m < 4; ++m)
; #pragma unroll
;                 for (int n = 0; n < 2; ++n) acc[a][b][m][n] = (f32x4){0.f, 0.f, 0.f, 0.f};
;     s16x8 At[4][2], B0[2][2], B1[2][2];
;     const char* cA = (const char*)(g.A + (long)cur.z * g.zA) + (size_t)cur.pm * tA; const char* cB = (const char*)(g.Bt + (long)cur.z * g.zB) + (size_t)cur.pn * tB;
;     PG8_STAGE(PG8_SB(0, 0), cB, voffB); PG8_STAGE(PG8_SB(0, 1), cB + hB, voffB); PG8_STAGE(PG8_SA(0, 0), cA, voffA); PG8_STAGE(PG8_SA(0, 1), cA + hA, voffA);
;     if (wr == 1) PG8_BAR;
; __device__ __forceinline__ void small_from_hn(const h16* __restrict__ hn, const h16* __restrict__ wsm16  , const float* __restrict__ fox_bf, const float* __restrict__ ml_bi, ...
;     ...
;     asm volatile("s_waitcnt vmcnt(0) lgkmcnt(0)" ::: "memory"); __syncthreads();
.LBB0_971:
	s_or_b64 exec, exec, s[14:15]
	s_waitcnt lgkmcnt(0)
	v_readlane_b32 s0, v254, 6
	v_mov_b32_e32 v14, v243
	v_readlane_b32 s1, v254, 7
	s_barrier
	s_andn2_b64 vcc, exec, s[0:1]
	v_readfirstlane_b32 s14, v14
	s_cbranch_vccnz .LBB0_987
	v_lshlrev_b32_e32 v0, 4, v14
	v_add_u32_e32 v1, 0x2000, v0
	v_ashrrev_i32_e32 v2, 31, v1
	v_lshrrev_b32_e32 v2, 22, v2
	v_add_u32_e32 v2, v1, v2
	v_ashrrev_i32_e32 v8, 10, v2
	v_mul_i32_i24_e32 v2, 0x400, v8
	v_sub_u32_e32 v1, v1, v2
	v_lshrrev_b32_e32 v2, 4, v1
	v_bitop3_b32 v1, v2, v1, 32 bitop3:0x6c
	v_ashrrev_i32_e32 v2, 31, v1
	v_readlane_b32 s0, v255, 36
	v_lshrrev_b32_e32 v2, 26, v2
	v_readlane_b32 s1, v255, 37
	s_mov_b32 s4, s0
	v_add_u32_e32 v2, v1, v2
	v_lshlrev_b32_e32 v3, 3, v8
	s_mul_i32 s1, s4, 0x1200000
	v_readlane_b32 s4, v254, 4
	v_ashrrev_i32_e32 v9, 6, v2
	v_and_b32_e32 v3, -16, v3
	s_mul_hi_u32 s0, s0, 0x1200000
	v_readlane_b32 s5, v254, 5
	s_add_u32 s4, s4, s1
	v_add_u32_e32 v3, v9, v3
	s_addc_u32 s5, s5, s0
	v_and_b32_e32 v4, 3, v9
	s_mov_b32 s0, 0x1fffe0
	v_lshrrev_b32_e32 v5, 2, v3
	v_lshlrev_b32_e32 v6, 1, v3
	v_and_or_b32 v4, v3, s0, v4
	v_and_b32_e32 v5, 4, v5
	v_and_b32_e32 v6, 24, v6
	v_and_b32_e32 v2, 0xc0, v2
	v_or3_b32 v4, v4, v5, v6
	v_sub_u32_e32 v1, v1, v2
	v_mov_b32_e32 v6, 1
	v_lshlrev_b32_e32 v5, 5, v8
	v_ashrrev_i16_sdwa v1, v6, sext(v1) dst_sel:DWORD dst_unused:UNUSED_PAD src0_sel:DWORD src1_sel:BYTE_0
	v_and_b32_e32 v5, 32, v5
	v_bfe_i32 v10, v1, 0, 16
	v_add_lshl_u32 v1, v5, v10, 1
	v_lshl_add_u32 v130, v4, 11, v1
	v_and_b32_e32 v218, 0x30000, v130
	v_add_u32_e32 v130, v130, v218
	v_lshl_add_u32 v132, v3, 11, v1
	v_bfe_i32 v1, v14, 27, 1
	v_lshrrev_b32_e32 v1, 22, v1
	v_add_u32_e32 v1, v0, v1
	v_and_b32_e32 v1, 0xfffffc00, v1
	v_sub_u32_e32 v0, v0, v1
	v_lshrrev_b32_e32 v1, 4, v0
	v_ashrrev_i32_e32 v2, 31, v14
	v_bitop3_b32 v0, v1, v0, 32 bitop3:0x6c
	v_lshrrev_b32_e32 v2, 26, v2
	v_ashrrev_i32_e32 v1, 31, v0
	v_add_u32_e32 v2, v14, v2
	v_lshrrev_b32_e32 v1, 26, v1
	v_ashrrev_i32_e32 v12, 6, v2
	v_add_u32_e32 v1, v0, v1
	v_lshlrev_b32_e32 v2, 3, v12
	v_ashrrev_i32_e32 v11, 6, v1
	v_and_b32_e32 v2, -16, v2
	v_add_u32_e32 v2, v11, v2
	v_and_b32_e32 v3, 3, v11
	v_lshrrev_b32_e32 v4, 2, v2
	v_lshlrev_b32_e32 v5, 1, v2
	v_and_b32_e32 v1, 0xc0, v1
	s_ashr_i32 s15, s14, 6
	v_and_or_b32 v3, v2, s0, v3
	v_and_b32_e32 v4, 4, v4
	v_and_b32_e32 v5, 24, v5
	v_sub_u32_e32 v0, v0, v1
	s_ashr_i32 s19, s14, 8
	s_lshl_b32 s6, s15, 10
	v_or3_b32 v3, v3, v4, v5
	v_lshlrev_b32_e32 v4, 5, v12
	v_ashrrev_i16_sdwa v0, v6, sext(v0) dst_sel:DWORD dst_unused:UNUSED_PAD src0_sel:DWORD src1_sel:BYTE_0
	v_readlane_b32 s0, v254, 55
	v_and_b32_e32 v4, 32, v4
	v_bfe_i32 v13, v0, 0, 16
	v_readlane_b32 s1, v254, 56
	s_add_u32 s52, s4, s0
	v_add_lshl_u32 v0, v4, v13, 1
	s_addc_u32 s53, s5, s1
	s_add_i32 s10, s6, 0
	v_lshl_add_u32 v96, v3, 11, v0
	v_and_b32_e32 v218, 0x30000, v96
	v_add_u32_e32 v96, v96, v218
	s_add_i32 m0, s10, 0x10000
	v_lshl_add_u32 v134, v2, 11, v0
	global_load_lds_dwordx4 v96, s[52:53]
	s_add_i32 m0, s10, 0x12000
	s_add_u32 s0, s52, 0x10000
	global_load_lds_dwordx4 v130, s[52:53]
	s_addc_u32 s1, s53, 0
	s_add_i32 m0, s10, 0x14000
	v_mov_b32_e32 v131, v97
	global_load_lds_dwordx4 v96, s[0:1]
	s_add_i32 m0, s10, 0x16000
	v_mov_b32_e32 v135, v97
	global_load_lds_dwordx4 v130, s[0:1]
	v_readlane_b32 s0, v255, 9
	v_readlane_b32 s1, v255, 10
	s_add_u32 s50, s2, s0
	s_addc_u32 s51, s3, s1
	s_add_i32 s11, s10, 0x2000
	s_mov_b32 m0, s10
	s_add_u32 s0, s50, 0x40000
	global_load_lds_dwordx4 v134, s[50:51]
	s_mov_b32 m0, s11
	s_addc_u32 s1, s51, 0
	s_add_i32 s12, s10, 0x4000
	global_load_lds_dwordx4 v132, s[50:51]
	s_mov_b32 m0, s12
	s_add_i32 s13, s10, 0x6000
	global_load_lds_dwordx4 v134, s[0:1]
	s_mov_b32 m0, s13
	v_mov_b32_e32 v133, v97
	global_load_lds_dwordx4 v132, s[0:1]
	v_readlane_b32 s0, v252, 14
	v_readlane_b32 s1, v252, 15
	s_load_dword s18, s[0:1], 0x0
	s_cmp_eq_u32 s19, 1
	v_lshl_add_u64 v[6:7], s[52:53], 0, v[96:97]
	v_lshl_add_u64 v[4:5], s[52:53], 0, v[130:131]
	v_lshl_add_u64 v[0:1], s[50:51], 0, v[134:135]
	s_cselect_b64 s[0:1], -1, 0
	s_cmp_lg_u32 s19, 1
	v_lshl_add_u64 v[2:3], s[50:51], 0, v[132:133]
	s_cbranch_scc1 .LBB0_974
	s_barrier
